# v17 + MLA attention: waves skip Q.K^T and P.V matrix work of key tiles lying entirely above their query rows (mask overwrites every score; P = 0)
# speedup vs baseline: 1.0043x; 1.0043x over previous
.LBB0_946:
	s_sub_i32 s1, s37, 94
	s_cmp_gt_i32 s1, s35
	s_cbranch_scc1 .Lmla_qkskip1
	s_lshl_b32 s50, s0, 14
	s_add_i32 s1, s50, 0
	v_add_u32_e32 v210, s1, v202
	ds_read_b128 v[98:101], v210 offset:49152
	ds_read_b128 v[102:105], v210 offset:57344
	v_xor_b32_e32 v210, 0x80, v210
	v_max_f32_e32 v186, v67, v67
	v_max_f32_e32 v187, v66, v66
	v_max_f32_e32 v186, v187, v186
	s_waitcnt lgkmcnt(1)
	v_mfma_f32_32x32x16_bf16 v[114:129], v[98:101], v[130:133], 0
	v_add_u32_e32 v212, s1, v207
	v_max3_f32 v186, v186, v68, v69
	ds_read_b128 v[178:181], v212 offset:49152
	ds_read_b128 v[182:185], v212 offset:57344
	v_xor_b32_e32 v212, 0x80, v212
	v_max3_f32 v186, v186, v70, v71
	v_max3_f32 v186, v186, v72, v73
	v_max3_f32 v186, v186, v74, v75
	v_max3_f32 v186, v186, v76, v77
	s_waitcnt lgkmcnt(2)
	v_mfma_f32_32x32x16_bf16 v[98:113], v[102:105], v[130:133], 0
	v_max3_f32 v186, v186, v78, v79
	v_lshl_add_u32 v211, s0, 13, v225
	v_max3_f32 v213, v186, v80, v81
	s_waitcnt lgkmcnt(1)
	v_mfma_f32_32x32x16_bf16 v[114:129], v[178:181], v[134:137], v[114:129]
	v_max3_f32 v178, v213, v82, v83
	v_max3_f32 v178, v178, v84, v85
	v_max3_f32 v178, v178, v86, v87
	v_max3_f32 v178, v178, v88, v89
	v_max3_f32 v178, v178, v90, v91
	v_max3_f32 v178, v178, v92, v93
	v_max3_f32 v178, v178, v94, v95
	v_max3_f32 v178, v178, v96, v97
	v_mov_b32_e32 v179, v178
	s_nop 1
	v_permlane32_swap_b32_e32 v178, v179
	v_max_f32_e32 v179, v179, v179
	v_max_f32_e32 v178, v178, v178
	v_max_f32_e32 v178, v178, v179
	v_sub_f32_e32 v179, v178, v231
	v_mul_f32_e32 v179, 0x3d93cd3a, v179
	v_cmp_ge_f32_e32 vcc, s36, v179
	s_cmp_eq_u64 vcc, exec
	v_max_f32_e32 v179, v231, v231
	s_waitcnt lgkmcnt(0)
	v_mfma_f32_32x32x16_bf16 v[98:113], v[182:185], v[134:137], v[98:113]
	s_cselect_b64 vcc, -1, 0
	v_max_f32_e32 v178, v179, v178
	v_cndmask_b32_e32 v232, v178, v231, vcc
	v_add_u32_e32 v218, s1, v209
	v_sub_f32_e32 v178, v231, v232
	ds_read_b128 v[186:189], v218 offset:49152
	ds_read_b128 v[190:193], v218 offset:57344
	v_xor_b32_e32 v218, 0x80, v218
	v_mul_f32_e32 v178, 0x3dd53b94, v178
	v_exp_f32_e32 v231, v178
	v_mul_f32_e32 v213, 0xbdd53b94, v232
	v_fmamk_f32 v66, v66, 0x3dd53b94, v213
	s_waitcnt lgkmcnt(1)
	v_mfma_f32_32x32x16_bf16 v[114:129], v[186:189], v[138:141], v[114:129]
	v_exp_f32_e32 v66, v66
	v_fmamk_f32 v82, v82, 0x3dd53b94, v213
	v_add_u32_e32 v219, s1, v224
	v_exp_f32_e32 v82, v82
	v_fmamk_f32 v67, v67, 0x3dd53b94, v213
	ds_read_b128 v[178:181], v219 offset:49152
	ds_read_b128 v[182:185], v219 offset:57344
	v_xor_b32_e32 v219, 0x80, v219
	v_exp_f32_e32 v67, v67
	s_waitcnt lgkmcnt(2)
	v_mfma_f32_32x32x16_bf16 v[98:113], v[190:193], v[138:141], v[98:113]
	v_fmamk_f32 v83, v83, 0x3dd53b94, v213
	v_exp_f32_e32 v83, v83
	v_add_f32_e32 v186, 0, v66
	v_add_f32_e32 v186, v82, v186
	v_add_f32_e32 v186, v67, v186
	v_add_f32_e32 v220, v83, v186
	v_fmamk_f32 v68, v68, 0x3dd53b94, v213
	s_waitcnt lgkmcnt(1)
	v_mfma_f32_32x32x16_bf16 v[114:129], v[178:181], v[142:145], v[114:129]
	v_exp_f32_e32 v68, v68
	v_fmamk_f32 v84, v84, 0x3dd53b94, v213
	v_exp_f32_e32 v84, v84
	v_fmamk_f32 v69, v69, 0x3dd53b94, v213
	ds_read_b128 v[186:189], v210 offset:49152
	ds_read_b128 v[190:193], v210 offset:57344
	v_exp_f32_e32 v69, v69
	v_fmamk_f32 v85, v85, 0x3dd53b94, v213
	s_waitcnt lgkmcnt(2)
	v_mfma_f32_32x32x16_bf16 v[98:113], v[182:185], v[142:145], v[98:113]
	v_exp_f32_e32 v85, v85
	v_add_f32_e32 v178, v68, v220
	v_add_f32_e32 v178, v84, v178
	v_add_f32_e32 v178, v69, v178
	v_add_f32_e32 v210, v85, v178
	v_fmamk_f32 v70, v70, 0x3dd53b94, v213
	s_waitcnt lgkmcnt(1)
	v_mfma_f32_32x32x16_bf16 v[114:129], v[186:189], v[146:149], v[114:129]
	v_exp_f32_e32 v70, v70
	v_fmamk_f32 v86, v86, 0x3dd53b94, v213
	v_exp_f32_e32 v86, v86
	v_fmamk_f32 v71, v71, 0x3dd53b94, v213
	ds_read_b128 v[178:181], v212 offset:49152
	ds_read_b128 v[182:185], v212 offset:57344
	v_exp_f32_e32 v71, v71
	v_fmamk_f32 v87, v87, 0x3dd53b94, v213
	s_waitcnt lgkmcnt(2)
	v_mfma_f32_32x32x16_bf16 v[98:113], v[190:193], v[146:149], v[98:113]
	v_exp_f32_e32 v87, v87
	v_add_f32_e32 v186, v70, v210
	v_add_f32_e32 v186, v86, v186
	v_add_f32_e32 v186, v71, v186
	v_add_f32_e32 v210, v87, v186
	v_fmamk_f32 v72, v72, 0x3dd53b94, v213
	s_waitcnt lgkmcnt(1)
	v_mfma_f32_32x32x16_bf16 v[114:129], v[178:181], v[150:153], v[114:129]
	v_exp_f32_e32 v72, v72
	v_fmamk_f32 v88, v88, 0x3dd53b94, v213
	v_exp_f32_e32 v88, v88
	v_fmamk_f32 v73, v73, 0x3dd53b94, v213
	ds_read_b128 v[186:189], v218 offset:49152
	ds_read_b128 v[190:193], v218 offset:57344
	v_exp_f32_e32 v73, v73
	v_fmamk_f32 v89, v89, 0x3dd53b94, v213
	s_waitcnt lgkmcnt(2)
	v_mfma_f32_32x32x16_bf16 v[98:113], v[182:185], v[150:153], v[98:113]
	v_exp_f32_e32 v89, v89
	v_add_f32_e32 v178, v72, v210
	v_add_f32_e32 v178, v88, v178
	v_add_f32_e32 v178, v73, v178
	v_add_f32_e32 v210, v89, v178
	v_fmamk_f32 v74, v74, 0x3dd53b94, v213
	v_exp_f32_e32 v74, v74
	v_fmamk_f32 v90, v90, 0x3dd53b94, v213
	s_waitcnt lgkmcnt(1)
	v_mfma_f32_32x32x16_bf16 v[114:129], v[186:189], v[154:157], v[114:129]
	v_exp_f32_e32 v90, v90
	v_fmamk_f32 v75, v75, 0x3dd53b94, v213
	v_exp_f32_e32 v75, v75
	v_fmamk_f32 v91, v91, 0x3dd53b94, v213
	ds_read_b128 v[178:181], v219 offset:49152
	ds_read_b128 v[182:185], v219 offset:57344
	v_exp_f32_e32 v91, v91
	v_add_f32_e32 v186, v74, v210
	s_waitcnt lgkmcnt(2)
	v_mfma_f32_32x32x16_bf16 v[98:113], v[190:193], v[154:157], v[98:113]
	v_add_f32_e32 v186, v90, v186
	v_add_f32_e32 v186, v75, v186
	v_add_f32_e32 v190, v91, v186
	v_fmamk_f32 v76, v76, 0x3dd53b94, v213
	v_exp_f32_e32 v76, v76
	v_fmamk_f32 v92, v92, 0x3dd53b94, v213
	s_waitcnt lgkmcnt(1)
	v_mfma_f32_32x32x16_bf16 v[114:129], v[178:181], v[158:161], v[114:129]
	v_exp_f32_e32 v92, v92
	v_fmamk_f32 v77, v77, 0x3dd53b94, v213
	v_add_u32_e32 v186, v211, v226
	v_exp_f32_e32 v77, v77
	v_fmamk_f32 v93, v93, 0x3dd53b94, v213
	ds_read_b128 v[178:181], v186
	ds_read_b128 v[186:189], v186 offset:4096
	v_exp_f32_e32 v93, v93
	s_waitcnt lgkmcnt(2)
	v_mfma_f32_32x32x16_bf16 v[98:113], v[182:185], v[158:161], v[98:113]
	v_add_f32_e32 v190, v76, v190
	v_add_f32_e32 v190, v92, v190
	v_add_f32_e32 v182, v77, v190
	v_add_f32_e32 v190, v93, v182
	v_fmamk_f32 v78, v78, 0x3dd53b94, v213
	v_exp_f32_e32 v78, v78
	v_fmamk_f32 v94, v94, 0x3dd53b94, v213
	s_waitcnt lgkmcnt(1)
	v_mfma_f32_32x32x16_bf16 v[114:129], v[178:181], v[162:165], v[114:129]
	v_exp_f32_e32 v94, v94
	v_fmamk_f32 v79, v79, 0x3dd53b94, v213
	v_add_u32_e32 v182, v211, v206
	v_exp_f32_e32 v79, v79
	v_fmamk_f32 v95, v95, 0x3dd53b94, v213
	ds_read_b128 v[178:181], v182
	ds_read_b128 v[182:185], v182 offset:4096
	v_exp_f32_e32 v95, v95
	s_waitcnt lgkmcnt(2)
	v_mfma_f32_32x32x16_bf16 v[98:113], v[186:189], v[162:165], v[98:113]
	v_add_f32_e32 v190, v78, v190
	v_add_f32_e32 v190, v94, v190
	v_add_f32_e32 v186, v79, v190
	v_add_f32_e32 v190, v95, v186
	v_fmamk_f32 v80, v80, 0x3dd53b94, v213
	v_exp_f32_e32 v80, v80
	v_fmamk_f32 v96, v96, 0x3dd53b94, v213
	s_waitcnt lgkmcnt(1)
	v_mfma_f32_32x32x16_bf16 v[114:129], v[178:181], v[166:169], v[114:129]
	v_exp_f32_e32 v96, v96
	v_fmamk_f32 v81, v81, 0x3dd53b94, v213
	v_add_u32_e32 v186, v211, v208
	v_exp_f32_e32 v81, v81
	v_fmac_f32_e32 v213, 0x3dd53b94, v97
	ds_read_b128 v[178:181], v186
	ds_read_b128 v[186:189], v186 offset:4096
	v_exp_f32_e32 v97, v213
	s_waitcnt lgkmcnt(2)
	v_mfma_f32_32x32x16_bf16 v[98:113], v[182:185], v[166:169], v[98:113]
	v_add_f32_e32 v190, v80, v190
	v_add_f32_e32 v190, v96, v190
	v_add_f32_e32 v182, v81, v190
	v_add_f32_e32 v233, v97, v182
	s_waitcnt lgkmcnt(1)
	v_mfma_f32_32x32x16_bf16 v[114:129], v[178:181], v[170:173], v[114:129]
	v_add_u32_e32 v182, v211, v223
	ds_read_b128 v[190:193], v182
	ds_read_b128 v[236:239], v182 offset:4096
	v_mov_b32_e32 v234, v233
	v_cvt_pk_bf16_f32 v178, v66, v67
	v_cvt_pk_bf16_f32 v179, v68, v69
	v_cvt_pk_bf16_f32 v180, v70, v71
	v_cvt_pk_bf16_f32 v181, v72, v73
	s_waitcnt lgkmcnt(2)
	v_mfma_f32_32x32x16_bf16 v[98:113], v[186:189], v[170:173], v[98:113]
	v_cvt_pk_bf16_f32 v182, v74, v75
	v_cvt_pk_bf16_f32 v183, v76, v77
	v_cvt_pk_bf16_f32 v184, v78, v79
	v_cvt_pk_bf16_f32 v185, v80, v81
	v_permlane32_swap_b32_e32 v233, v234
	v_permlane32_swap_b32_e32 v178, v180
	v_permlane32_swap_b32_e32 v179, v181
	v_permlane32_swap_b32_e32 v182, v184
	v_permlane32_swap_b32_e32 v183, v185
	s_waitcnt lgkmcnt(1)
	v_mfma_f32_32x32x16_bf16 v[114:129], v[190:193], v[174:177], v[114:129]
	v_cvt_pk_bf16_f32 v186, v82, v83
	v_cvt_pk_bf16_f32 v187, v84, v85
	v_cvt_pk_bf16_f32 v188, v86, v87
	v_cvt_pk_bf16_f32 v189, v88, v89
	v_cvt_pk_bf16_f32 v190, v90, v91
	v_cvt_pk_bf16_f32 v191, v92, v93
	v_cvt_pk_bf16_f32 v192, v94, v95
	s_waitcnt lgkmcnt(0)
	v_mfma_f32_32x32x16_bf16 v[98:113], v[236:239], v[174:177], v[98:113]
	v_cvt_pk_bf16_f32 v193, v96, v97
	v_permlane32_swap_b32_e32 v186, v188
	v_permlane32_swap_b32_e32 v187, v189
	v_permlane32_swap_b32_e32 v190, v192
	v_permlane32_swap_b32_e32 v191, v193
.Lmla_qk1_join:
	v_cmp_gt_f32_e32 vcc, 1.0, v231
	s_cbranch_vccz .LBB0_950
	s_and_saveexec_b64 s[46:47], s[2:3]
	ds_write_b32 v227, v231 offset:128
	s_or_b64 exec, exec, s[46:47]
	s_waitcnt lgkmcnt(0)
	ds_read_b128 v[236:239], v1 offset:224
	ds_read_b128 v[240:243], v1 offset:192
	ds_read_b128 v[244:247], v1 offset:160
	ds_read_b128 v[218:221], v1 offset:128
	s_waitcnt lgkmcnt(3)
	v_pk_mul_f32 v[64:65], v[64:65], v[238:239]
	s_waitcnt lgkmcnt(2)
	v_pk_mul_f32 v[60:61], v[60:61], v[242:243]
	s_waitcnt lgkmcnt(1)
	v_pk_mul_f32 v[56:57], v[56:57], v[246:247]
	s_waitcnt lgkmcnt(0)
	v_pk_mul_f32 v[52:53], v[52:53], v[220:221]
	v_pk_mul_f32 v[62:63], v[62:63], v[236:237]
	v_pk_mul_f32 v[58:59], v[58:59], v[240:241]
	v_pk_mul_f32 v[54:55], v[54:55], v[244:245]
	v_pk_mul_f32 v[50:51], v[50:51], v[218:219]
	v_pk_mul_f32 v[48:49], v[48:49], v[238:239]
	v_pk_mul_f32 v[44:45], v[44:45], v[242:243]
	v_pk_mul_f32 v[40:41], v[40:41], v[246:247]
	v_pk_mul_f32 v[36:37], v[36:37], v[220:221]
	v_pk_mul_f32 v[46:47], v[46:47], v[236:237]
	v_pk_mul_f32 v[42:43], v[42:43], v[240:241]
	v_pk_mul_f32 v[38:39], v[38:39], v[244:245]
	v_pk_mul_f32 v[34:35], v[34:35], v[218:219]
	v_pk_mul_f32 v[32:33], v[32:33], v[238:239]
	v_pk_mul_f32 v[28:29], v[28:29], v[242:243]
	v_pk_mul_f32 v[24:25], v[24:25], v[246:247]
	v_pk_mul_f32 v[20:21], v[20:21], v[220:221]
	v_pk_mul_f32 v[30:31], v[30:31], v[236:237]
	v_pk_mul_f32 v[26:27], v[26:27], v[240:241]
	v_pk_mul_f32 v[22:23], v[22:23], v[244:245]
	v_pk_mul_f32 v[18:19], v[18:19], v[218:219]
	v_pk_mul_f32 v[16:17], v[16:17], v[238:239]
	v_pk_mul_f32 v[12:13], v[12:13], v[242:243]
	v_pk_mul_f32 v[8:9], v[8:9], v[246:247]
	v_pk_mul_f32 v[4:5], v[4:5], v[220:221]
	v_pk_mul_f32 v[14:15], v[14:15], v[236:237]
	v_pk_mul_f32 v[10:11], v[10:11], v[240:241]
	v_pk_mul_f32 v[6:7], v[6:7], v[244:245]
	v_pk_mul_f32 v[2:3], v[2:3], v[218:219]
.LBB0_950:
	s_sub_i32 s1, s37, 0x9e
	s_cmp_gt_i32 s1, s35
	s_cbranch_scc1 .Lmla_pvskip1
	s_lshl_b32 s0, s40, 14
	v_add_u32_e32 v210, s0, v228
	ds_read_b64_tr_b16 v[218:219], v210 offset:0
	ds_read_b64_tr_b16 v[220:221], v210 offset:0x800
	ds_read_b64_tr_b16 v[236:237], v210 offset:0x1000
	ds_read_b64_tr_b16 v[238:239], v210 offset:0x1800
	ds_read_b64_tr_b16 v[240:241], v210 offset:0x2000
	ds_read_b64_tr_b16 v[242:243], v210 offset:0x2800
	ds_read_b64_tr_b16 v[244:245], v210 offset:0x3000
	ds_read_b64_tr_b16 v[246:247], v210 offset:0x3800
	s_waitcnt lgkmcnt(0)
	s_nop 0
	v_mfma_f32_32x32x16_bf16 v[50:65], v[178:181], v[218:221], v[50:65]
	ds_read_b64_tr_b16 v[218:219], v210 offset:0x200
	ds_read_b64_tr_b16 v[220:221], v210 offset:0xa00
	v_mfma_f32_32x32x16_bf16 v[50:65], v[182:185], v[236:239], v[50:65]
	ds_read_b64_tr_b16 v[236:237], v210 offset:0x1200
	ds_read_b64_tr_b16 v[238:239], v210 offset:0x1a00
	v_mfma_f32_32x32x16_bf16 v[50:65], v[186:189], v[240:243], v[50:65]
	ds_read_b64_tr_b16 v[240:241], v210 offset:0x2200
	ds_read_b64_tr_b16 v[242:243], v210 offset:0x2a00
	v_mfma_f32_32x32x16_bf16 v[50:65], v[190:193], v[244:247], v[50:65]
	ds_read_b64_tr_b16 v[244:245], v210 offset:0x3200
	ds_read_b64_tr_b16 v[246:247], v210 offset:0x3a00
	s_waitcnt lgkmcnt(0)
	v_mfma_f32_32x32x16_bf16 v[34:49], v[178:181], v[218:221], v[34:49]
	ds_read_b64_tr_b16 v[218:219], v210 offset:0x400
	ds_read_b64_tr_b16 v[220:221], v210 offset:0xc00
	v_mfma_f32_32x32x16_bf16 v[34:49], v[182:185], v[236:239], v[34:49]
	ds_read_b64_tr_b16 v[236:237], v210 offset:0x1400
	ds_read_b64_tr_b16 v[238:239], v210 offset:0x1c00
	v_mfma_f32_32x32x16_bf16 v[34:49], v[186:189], v[240:243], v[34:49]
	ds_read_b64_tr_b16 v[240:241], v210 offset:0x2400
	ds_read_b64_tr_b16 v[242:243], v210 offset:0x2c00
	v_mfma_f32_32x32x16_bf16 v[34:49], v[190:193], v[244:247], v[34:49]
	ds_read_b64_tr_b16 v[244:245], v210 offset:0x3400
	ds_read_b64_tr_b16 v[246:247], v210 offset:0x3c00
	s_waitcnt lgkmcnt(0)
	v_mfma_f32_32x32x16_bf16 v[18:33], v[178:181], v[218:221], v[18:33]
	ds_read_b64_tr_b16 v[218:219], v210 offset:0x600
	ds_read_b64_tr_b16 v[220:221], v210 offset:0xe00
	v_mfma_f32_32x32x16_bf16 v[18:33], v[182:185], v[236:239], v[18:33]
	ds_read_b64_tr_b16 v[236:237], v210 offset:0x1600
	ds_read_b64_tr_b16 v[238:239], v210 offset:0x1e00
	v_mfma_f32_32x32x16_bf16 v[18:33], v[186:189], v[240:243], v[18:33]
	ds_read_b64_tr_b16 v[240:241], v210 offset:0x2600
	ds_read_b64_tr_b16 v[242:243], v210 offset:0x2e00
	v_mfma_f32_32x32x16_bf16 v[18:33], v[190:193], v[244:247], v[18:33]
	ds_read_b64_tr_b16 v[244:245], v210 offset:0x3600
	ds_read_b64_tr_b16 v[246:247], v210 offset:0x3e00
	s_waitcnt lgkmcnt(0)
	v_mfma_f32_32x32x16_bf16 v[2:17], v[178:181], v[218:221], v[2:17]
	s_waitcnt vmcnt(0)
	s_cmp_ge_u32 s34, s21
	s_barrier
	v_mfma_f32_32x32x16_bf16 v[2:17], v[182:185], v[236:239], v[2:17]
	v_mfma_f32_32x32x16_bf16 v[2:17], v[186:189], v[240:243], v[2:17]
	v_mfma_f32_32x32x16_bf16 v[2:17], v[190:193], v[244:247], v[2:17]
.Lmla_pv1_end:
	s_cbranch_scc1 .LBB0_952
	s_add_i32 s1, s0, s19
	s_mov_b32 m0, s1
	s_nop 0
	global_load_lds_dwordx4 v198, s[22:23]
	s_addk_i32 s1, 0x400
	s_mov_b32 m0, s1
	s_nop 0
	global_load_lds_dwordx4 v200, s[22:23]
	s_add_i32 s0, s0, s17
	s_mov_b32 m0, s0
	s_nop 0
	global_load_lds_dwordx4 v197, s[22:23]
	s_addk_i32 s0, 0x400
	s_mov_b32 m0, s0
	s_nop 0
	global_load_lds_dwordx4 v199, s[22:23]
	s_lshl_b32 s0, s40, 13
	s_add_i32 s0, s0, s18
	s_mov_b32 m0, s0
	s_nop 0
	global_load_lds_dwordx4 v201, s[42:43]

.LBB0_954:
	v_add_f32_e32 v233, v233, v234
	v_fmac_f32_e32 v233, v230, v231
	s_mov_b64 s[40:41], -1
	s_and_b64 vcc, exec, s[44:45]
	v_max_f32_e32 v235, v232, v232
	v_max_f32_e32 v236, v115, v115
	v_max_f32_e32 v237, v114, v114
	s_cbranch_vccnz .LBB0_957
	s_sub_i32 s1, s37, 30
	s_cmp_gt_i32 s1, s35
	s_cbranch_scc1 .LBB0_957
	s_andn2_b64 vcc, exec, s[40:41]
	s_cbranch_vccz .LBB0_958

.LBB0_962:
	s_sub_i32 s1, s37, 94
	s_cmp_gt_i32 s1, s35
	s_cbranch_scc1 .Lmla_pvskip2
	v_add_u32_e32 v114, s50, v228
	ds_read_b64_tr_b16 v[98:99], v114 offset:0
	ds_read_b64_tr_b16 v[100:101], v114 offset:0x800
	ds_read_b64_tr_b16 v[102:103], v114 offset:0x1000
	ds_read_b64_tr_b16 v[104:105], v114 offset:0x1800
	ds_read_b64_tr_b16 v[106:107], v114 offset:0x2000
	ds_read_b64_tr_b16 v[108:109], v114 offset:0x2800
	ds_read_b64_tr_b16 v[110:111], v114 offset:0x3000
	ds_read_b64_tr_b16 v[112:113], v114 offset:0x3800
	s_waitcnt lgkmcnt(0)
	s_nop 0
	v_mfma_f32_32x32x16_bf16 v[50:65], v[178:181], v[98:101], v[50:65]
	ds_read_b64_tr_b16 v[98:99], v114 offset:0x200
	ds_read_b64_tr_b16 v[100:101], v114 offset:0xa00
	v_mfma_f32_32x32x16_bf16 v[50:65], v[182:185], v[102:105], v[50:65]
	ds_read_b64_tr_b16 v[102:103], v114 offset:0x1200
	ds_read_b64_tr_b16 v[104:105], v114 offset:0x1a00
	v_mfma_f32_32x32x16_bf16 v[50:65], v[186:189], v[106:109], v[50:65]
	ds_read_b64_tr_b16 v[106:107], v114 offset:0x2200
	ds_read_b64_tr_b16 v[108:109], v114 offset:0x2a00
	v_mfma_f32_32x32x16_bf16 v[50:65], v[190:193], v[110:113], v[50:65]
	ds_read_b64_tr_b16 v[110:111], v114 offset:0x3200
	ds_read_b64_tr_b16 v[112:113], v114 offset:0x3a00
	s_waitcnt lgkmcnt(0)
	v_mfma_f32_32x32x16_bf16 v[34:49], v[178:181], v[98:101], v[34:49]
	ds_read_b64_tr_b16 v[98:99], v114 offset:0x400
	ds_read_b64_tr_b16 v[100:101], v114 offset:0xc00
	v_mfma_f32_32x32x16_bf16 v[34:49], v[182:185], v[102:105], v[34:49]
	ds_read_b64_tr_b16 v[102:103], v114 offset:0x1400
	ds_read_b64_tr_b16 v[104:105], v114 offset:0x1c00
	v_mfma_f32_32x32x16_bf16 v[34:49], v[186:189], v[106:109], v[34:49]
	ds_read_b64_tr_b16 v[106:107], v114 offset:0x2400
	ds_read_b64_tr_b16 v[108:109], v114 offset:0x2c00
	v_mfma_f32_32x32x16_bf16 v[34:49], v[190:193], v[110:113], v[34:49]
	ds_read_b64_tr_b16 v[110:111], v114 offset:0x3400
	ds_read_b64_tr_b16 v[112:113], v114 offset:0x3c00
	s_waitcnt lgkmcnt(0)
	v_mfma_f32_32x32x16_bf16 v[18:33], v[178:181], v[98:101], v[18:33]
	ds_read_b64_tr_b16 v[98:99], v114 offset:0x600
	ds_read_b64_tr_b16 v[100:101], v114 offset:0xe00
	v_mfma_f32_32x32x16_bf16 v[18:33], v[182:185], v[102:105], v[18:33]
	ds_read_b64_tr_b16 v[102:103], v114 offset:0x1600
	ds_read_b64_tr_b16 v[104:105], v114 offset:0x1e00
	v_mfma_f32_32x32x16_bf16 v[18:33], v[186:189], v[106:109], v[18:33]
	ds_read_b64_tr_b16 v[106:107], v114 offset:0x2600
	ds_read_b64_tr_b16 v[108:109], v114 offset:0x2e00
	v_mfma_f32_32x32x16_bf16 v[18:33], v[190:193], v[110:113], v[18:33]
	ds_read_b64_tr_b16 v[110:111], v114 offset:0x3600
	ds_read_b64_tr_b16 v[112:113], v114 offset:0x3e00
	s_waitcnt lgkmcnt(0)
	v_mfma_f32_32x32x16_bf16 v[2:17], v[178:181], v[98:101], v[2:17]
	s_add_u32 s42, s42, 0x4000
	s_addc_u32 s43, s43, 0
	s_waitcnt vmcnt(0)
	s_add_u32 s22, s22, 0x80000
	s_addc_u32 s23, s23, 0
	s_add_i32 s34, s34, 2
	s_addk_i32 s37, 0x80
	v_mfma_f32_32x32x16_bf16 v[2:17], v[182:185], v[102:105], v[2:17]
	v_add_u32_e32 v229, 0xffffff80, v229
	s_cmp_ge_u32 s49, s21
	s_barrier
	v_mfma_f32_32x32x16_bf16 v[2:17], v[186:189], v[106:109], v[2:17]
	v_mfma_f32_32x32x16_bf16 v[2:17], v[190:193], v[110:113], v[2:17]
.Lmla_pv2_end:
	s_cbranch_scc1 .LBB0_964
	s_mov_b32 s40, s48
	s_branch .LBB0_942
.Lmla_pvskip2:
	s_add_u32 s42, s42, 0x4000
	s_addc_u32 s43, s43, 0
	s_waitcnt vmcnt(0)
	s_add_u32 s22, s22, 0x80000
	s_addc_u32 s23, s23, 0
	s_add_i32 s34, s34, 2
	s_addk_i32 s37, 0x80
	v_add_u32_e32 v229, 0xffffff80, v229
	s_cmp_ge_u32 s49, s21
	s_barrier
	s_branch .Lmla_pv2_end
.Lmla_pvskip1:
	s_lshl_b32 s0, s40, 14
	s_waitcnt vmcnt(0)
	s_cmp_ge_u32 s34, s21
	s_barrier
	s_branch .Lmla_pv1_end
.Lmla_qkskip1:
	s_lshl_b32 s50, s0, 14
	s_add_i32 s1, s50, 0
	v_add_u32_e32 v210, s1, v202
	v_xor_b32_e32 v210, 0x80, v210
	v_max_f32_e32 v186, v67, v67
	v_max_f32_e32 v187, v66, v66
	v_max_f32_e32 v186, v187, v186
	v_add_u32_e32 v212, s1, v207
	v_max3_f32 v186, v186, v68, v69
	v_xor_b32_e32 v212, 0x80, v212
	v_max3_f32 v186, v186, v70, v71
	v_max3_f32 v186, v186, v72, v73
	v_max3_f32 v186, v186, v74, v75
	v_max3_f32 v186, v186, v76, v77
	v_max3_f32 v186, v186, v78, v79
	v_lshl_add_u32 v211, s0, 13, v225
	v_max3_f32 v213, v186, v80, v81
	v_max3_f32 v178, v213, v82, v83
	v_max3_f32 v178, v178, v84, v85
	v_max3_f32 v178, v178, v86, v87
	v_max3_f32 v178, v178, v88, v89
	v_max3_f32 v178, v178, v90, v91
	v_max3_f32 v178, v178, v92, v93
	v_max3_f32 v178, v178, v94, v95
	v_max3_f32 v178, v178, v96, v97
	v_mov_b32_e32 v179, v178
	s_nop 1
	v_permlane32_swap_b32_e32 v178, v179
	v_max_f32_e32 v179, v179, v179
	v_max_f32_e32 v178, v178, v178
	v_max_f32_e32 v178, v178, v179
	v_sub_f32_e32 v179, v178, v231
	v_mul_f32_e32 v179, 0x3d93cd3a, v179
	v_cmp_ge_f32_e32 vcc, s36, v179
	s_cmp_eq_u64 vcc, exec
	v_max_f32_e32 v179, v231, v231
	s_cselect_b64 vcc, -1, 0
	v_max_f32_e32 v178, v179, v178
	v_cndmask_b32_e32 v232, v178, v231, vcc
	v_add_u32_e32 v218, s1, v209
	v_sub_f32_e32 v178, v231, v232
	v_xor_b32_e32 v218, 0x80, v218
	v_mul_f32_e32 v178, 0x3dd53b94, v178
	v_exp_f32_e32 v231, v178
	v_mul_f32_e32 v213, 0xbdd53b94, v232
	v_fmamk_f32 v66, v66, 0x3dd53b94, v213
	v_exp_f32_e32 v66, v66
	v_fmamk_f32 v82, v82, 0x3dd53b94, v213
	v_add_u32_e32 v219, s1, v224
	v_exp_f32_e32 v82, v82
	v_fmamk_f32 v67, v67, 0x3dd53b94, v213
	v_xor_b32_e32 v219, 0x80, v219
	v_exp_f32_e32 v67, v67
	v_fmamk_f32 v83, v83, 0x3dd53b94, v213
	v_exp_f32_e32 v83, v83
	v_add_f32_e32 v186, 0, v66
	v_add_f32_e32 v186, v82, v186
	v_add_f32_e32 v186, v67, v186
	v_add_f32_e32 v220, v83, v186
	v_fmamk_f32 v68, v68, 0x3dd53b94, v213
	v_exp_f32_e32 v68, v68
	v_fmamk_f32 v84, v84, 0x3dd53b94, v213
	v_exp_f32_e32 v84, v84
	v_fmamk_f32 v69, v69, 0x3dd53b94, v213
	v_exp_f32_e32 v69, v69
	v_fmamk_f32 v85, v85, 0x3dd53b94, v213
	v_exp_f32_e32 v85, v85
	v_add_f32_e32 v178, v68, v220
	v_add_f32_e32 v178, v84, v178
	v_add_f32_e32 v178, v69, v178
	v_add_f32_e32 v210, v85, v178
	v_fmamk_f32 v70, v70, 0x3dd53b94, v213
	v_exp_f32_e32 v70, v70
	v_fmamk_f32 v86, v86, 0x3dd53b94, v213
	v_exp_f32_e32 v86, v86
	v_fmamk_f32 v71, v71, 0x3dd53b94, v213
	v_exp_f32_e32 v71, v71
	v_fmamk_f32 v87, v87, 0x3dd53b94, v213
	v_exp_f32_e32 v87, v87
	v_add_f32_e32 v186, v70, v210
	v_add_f32_e32 v186, v86, v186
	v_add_f32_e32 v186, v71, v186
	v_add_f32_e32 v210, v87, v186
	v_fmamk_f32 v72, v72, 0x3dd53b94, v213
	v_exp_f32_e32 v72, v72
	v_fmamk_f32 v88, v88, 0x3dd53b94, v213
	v_exp_f32_e32 v88, v88
	v_fmamk_f32 v73, v73, 0x3dd53b94, v213
	v_exp_f32_e32 v73, v73
	v_fmamk_f32 v89, v89, 0x3dd53b94, v213
	v_exp_f32_e32 v89, v89
	v_add_f32_e32 v178, v72, v210
	v_add_f32_e32 v178, v88, v178
	v_add_f32_e32 v178, v73, v178
	v_add_f32_e32 v210, v89, v178
	v_fmamk_f32 v74, v74, 0x3dd53b94, v213
	v_exp_f32_e32 v74, v74
	v_fmamk_f32 v90, v90, 0x3dd53b94, v213
	v_exp_f32_e32 v90, v90
	v_fmamk_f32 v75, v75, 0x3dd53b94, v213
	v_exp_f32_e32 v75, v75
	v_fmamk_f32 v91, v91, 0x3dd53b94, v213
	v_exp_f32_e32 v91, v91
	v_add_f32_e32 v186, v74, v210
	v_add_f32_e32 v186, v90, v186
	v_add_f32_e32 v186, v75, v186
	v_add_f32_e32 v190, v91, v186
	v_fmamk_f32 v76, v76, 0x3dd53b94, v213
	v_exp_f32_e32 v76, v76
	v_fmamk_f32 v92, v92, 0x3dd53b94, v213
	v_exp_f32_e32 v92, v92
	v_fmamk_f32 v77, v77, 0x3dd53b94, v213
	v_add_u32_e32 v186, v211, v226
	v_exp_f32_e32 v77, v77
	v_fmamk_f32 v93, v93, 0x3dd53b94, v213
	v_exp_f32_e32 v93, v93
	v_add_f32_e32 v190, v76, v190
	v_add_f32_e32 v190, v92, v190
	v_add_f32_e32 v182, v77, v190
	v_add_f32_e32 v190, v93, v182
	v_fmamk_f32 v78, v78, 0x3dd53b94, v213
	v_exp_f32_e32 v78, v78
	v_fmamk_f32 v94, v94, 0x3dd53b94, v213
	v_exp_f32_e32 v94, v94
	v_fmamk_f32 v79, v79, 0x3dd53b94, v213
	v_add_u32_e32 v182, v211, v206
	v_exp_f32_e32 v79, v79
	v_fmamk_f32 v95, v95, 0x3dd53b94, v213
	v_exp_f32_e32 v95, v95
	v_add_f32_e32 v190, v78, v190
	v_add_f32_e32 v190, v94, v190
	v_add_f32_e32 v186, v79, v190
	v_add_f32_e32 v190, v95, v186
	v_fmamk_f32 v80, v80, 0x3dd53b94, v213
	v_exp_f32_e32 v80, v80
	v_fmamk_f32 v96, v96, 0x3dd53b94, v213
	v_exp_f32_e32 v96, v96
	v_fmamk_f32 v81, v81, 0x3dd53b94, v213
	v_add_u32_e32 v186, v211, v208
	v_exp_f32_e32 v81, v81
	v_fmac_f32_e32 v213, 0x3dd53b94, v97
	v_exp_f32_e32 v97, v213
	v_add_f32_e32 v190, v80, v190
	v_add_f32_e32 v190, v96, v190
	v_add_f32_e32 v182, v81, v190
	v_add_f32_e32 v233, v97, v182
	v_add_u32_e32 v182, v211, v223
	v_mov_b32_e32 v234, v233
	v_cvt_pk_bf16_f32 v178, v66, v67
	v_cvt_pk_bf16_f32 v179, v68, v69
	v_cvt_pk_bf16_f32 v180, v70, v71
	v_cvt_pk_bf16_f32 v181, v72, v73
	v_cvt_pk_bf16_f32 v182, v74, v75
	v_cvt_pk_bf16_f32 v183, v76, v77
	v_cvt_pk_bf16_f32 v184, v78, v79
	v_cvt_pk_bf16_f32 v185, v80, v81
	v_permlane32_swap_b32_e32 v233, v234
	v_permlane32_swap_b32_e32 v178, v180
	v_permlane32_swap_b32_e32 v179, v181
	v_permlane32_swap_b32_e32 v182, v184
	v_permlane32_swap_b32_e32 v183, v185
	v_cvt_pk_bf16_f32 v186, v82, v83
	v_cvt_pk_bf16_f32 v187, v84, v85
	v_cvt_pk_bf16_f32 v188, v86, v87
	v_cvt_pk_bf16_f32 v189, v88, v89
	v_cvt_pk_bf16_f32 v190, v90, v91
	v_cvt_pk_bf16_f32 v191, v92, v93
	v_cvt_pk_bf16_f32 v192, v94, v95
	v_cvt_pk_bf16_f32 v193, v96, v97
	v_permlane32_swap_b32_e32 v186, v188
	v_permlane32_swap_b32_e32 v187, v189
	v_permlane32_swap_b32_e32 v190, v192
	v_permlane32_swap_b32_e32 v191, v193
	s_branch .Lmla_qk1_join
